# phase-5 expert-weight conversion bodies rewritten LDS-free (register transpose, dwordx4 loads and stores), waits independent of load/store retire order
# baseline (speedup 1.0000x reference)
; #define LAS __attribute__((address_space(3)))
; __device__ __forceinline__ float clamp8(float x) { return __builtin_amdgcn_fmed3f(x, -448.f, 448.f); }
; #define LDS_WAIT() asm volatile("s_waitcnt lgkmcnt(0)" ::: "memory")
; __device__ __forceinline__ void cvt_load(const CvtDesc& d, float (&t)[64], int lane) {
;     const float* p = d.src + (size_t)(lane >> 4) * d.N + 4 * (lane & 15);
; #pragma unroll
;     for (int i = 0; i < 16; ++i) { const f32x4 v = __builtin_nontemporal_load((const f32x4*)(p + (size_t)(4 * i) * d.N));
;         t[4 * i] = v.x; t[4 * i + 1] = v.y; t[4 * i + 2] = v.z; t[4 * i + 3] = v.w; }
; }
; __device__ __forceinline__ void cvt_finish(const CvtDesc& d, const float (&t)[64], LAS float* scr, int lane) {
;     LAS float* sw = scr + (lane >> 4) * 65 + 4 * (lane & 15);
; #pragma unroll
;     for (int i = 0; i < 16; ++i) { sw[(4 * i) * 65] = t[4 * i]; sw[(4 * i) * 65 + 1] = t[4 * i + 1]; sw[(4 * i) * 65 + 2] = t[4 * i + 2]; sw[(4 * i) * 65 + 3] = t[4 * i + 3]; }
;     LDS_WAIT();
;     const int c = lane & 7;
;     if (d.f8) {
; #pragma unroll
;         for (int j = 0; j < 8; ++j) { const int n = (lane >> 3) + 8 * j; const LAS float* s = scr + (8 * c) * 65 + n;
;             int a = __builtin_amdgcn_cvt_pk_fp8_f32(clamp8(s[0 * 65] * W8_SCALE), clamp8(s[1 * 65] * W8_SCALE), 0, false); a = __builtin_amdgcn_cvt_pk_fp8_f32(clamp8(s[2 * 65] * W8_SCALE), clamp8(s[3 * 65] * W8_SCALE), a, true);
;             int b = __builtin_amdgcn_cvt_pk_fp8_f32(clamp8(s[4 * 65] * W8_SCALE), clamp8(s[5 * 65] * W8_SCALE), 0, false); b = __builtin_amdgcn_cvt_pk_fp8_f32(clamp8(s[6 * 65] * W8_SCALE), clamp8(s[7 * 65] * W8_SCALE), b, true);
.Lcv_dd2:
	v_lshlrev_b32_e32 v166, 4, v165
	v_lshl_add_u32 v166, v164, s19, v166
	global_load_dwordx4 v[0:3], v166, s[10:11] nt
	v_add_u32_e32 v166, s15, v166
	global_load_dwordx4 v[4:7], v166, s[10:11] nt
	v_add_u32_e32 v166, s15, v166
	global_load_dwordx4 v[8:11], v166, s[10:11] nt
	v_add_u32_e32 v166, s15, v166
	global_load_dwordx4 v[12:15], v166, s[10:11] nt
	v_add_u32_e32 v166, s15, v166
	global_load_dwordx4 v[16:19], v166, s[10:11] nt
	v_add_u32_e32 v166, s15, v166
	global_load_dwordx4 v[20:23], v166, s[10:11] nt
	v_add_u32_e32 v166, s15, v166
	global_load_dwordx4 v[24:27], v166, s[10:11] nt
	v_add_u32_e32 v166, s15, v166
	global_load_dwordx4 v[28:31], v166, s[10:11] nt
	v_add_u32_e32 v166, s15, v166
	global_load_dwordx4 v[32:35], v166, s[10:11] nt
	v_add_u32_e32 v166, s15, v166
	global_load_dwordx4 v[36:39], v166, s[10:11] nt
	v_add_u32_e32 v166, s15, v166
	global_load_dwordx4 v[40:43], v166, s[10:11] nt
	v_add_u32_e32 v166, s15, v166
	global_load_dwordx4 v[44:47], v166, s[10:11] nt
	v_add_u32_e32 v166, s15, v166
	global_load_dwordx4 v[48:51], v166, s[10:11] nt
	v_add_u32_e32 v166, s15, v166
	global_load_dwordx4 v[52:55], v166, s[10:11] nt
	v_add_u32_e32 v166, s15, v166
	global_load_dwordx4 v[56:59], v166, s[10:11] nt
	v_add_u32_e32 v166, s15, v166
	global_load_dwordx4 v[60:63], v166, s[10:11] nt
	s_waitcnt vmcnt(16)
	v_mul_f32_e32 v64, 0x42800000, v64
	v_mul_f32_e32 v65, 0x42800000, v65
	v_mul_f32_e32 v66, 0x42800000, v66
	v_mul_f32_e32 v67, 0x42800000, v67
	v_mul_f32_e32 v68, 0x42800000, v68
	v_mul_f32_e32 v69, 0x42800000, v69
	v_mul_f32_e32 v70, 0x42800000, v70
	v_mul_f32_e32 v71, 0x42800000, v71
	v_mul_f32_e32 v72, 0x42800000, v72
	v_mul_f32_e32 v73, 0x42800000, v73
	v_mul_f32_e32 v74, 0x42800000, v74
	v_mul_f32_e32 v75, 0x42800000, v75
	v_mul_f32_e32 v76, 0x42800000, v76
	v_mul_f32_e32 v77, 0x42800000, v77
	v_mul_f32_e32 v78, 0x42800000, v78
	v_mul_f32_e32 v79, 0x42800000, v79
	v_mul_f32_e32 v80, 0x42800000, v80
	v_mul_f32_e32 v81, 0x42800000, v81
	v_mul_f32_e32 v82, 0x42800000, v82
	v_mul_f32_e32 v83, 0x42800000, v83
	v_mul_f32_e32 v84, 0x42800000, v84
	v_mul_f32_e32 v85, 0x42800000, v85
	v_mul_f32_e32 v86, 0x42800000, v86
	v_mul_f32_e32 v87, 0x42800000, v87
	v_mul_f32_e32 v88, 0x42800000, v88
	v_mul_f32_e32 v89, 0x42800000, v89
	v_mul_f32_e32 v90, 0x42800000, v90
	v_mul_f32_e32 v91, 0x42800000, v91
	v_mul_f32_e32 v92, 0x42800000, v92
	v_mul_f32_e32 v93, 0x42800000, v93
	v_mul_f32_e32 v94, 0x42800000, v94
	v_mul_f32_e32 v95, 0x42800000, v95
	v_mul_f32_e32 v96, 0x42800000, v96
	v_mul_f32_e32 v97, 0x42800000, v97
	v_mul_f32_e32 v98, 0x42800000, v98
	v_mul_f32_e32 v99, 0x42800000, v99
	v_mul_f32_e32 v100, 0x42800000, v100
	v_mul_f32_e32 v101, 0x42800000, v101
	v_mul_f32_e32 v102, 0x42800000, v102
	v_mul_f32_e32 v103, 0x42800000, v103
	v_mul_f32_e32 v104, 0x42800000, v104
	v_mul_f32_e32 v105, 0x42800000, v105
	v_mul_f32_e32 v106, 0x42800000, v106
	v_mul_f32_e32 v107, 0x42800000, v107
	v_mul_f32_e32 v108, 0x42800000, v108
	v_mul_f32_e32 v109, 0x42800000, v109
	v_mul_f32_e32 v110, 0x42800000, v110
	v_mul_f32_e32 v111, 0x42800000, v111
	v_mul_f32_e32 v112, 0x42800000, v112
	v_mul_f32_e32 v113, 0x42800000, v113
	v_mul_f32_e32 v114, 0x42800000, v114
	v_mul_f32_e32 v115, 0x42800000, v115
	v_mul_f32_e32 v116, 0x42800000, v116
	v_mul_f32_e32 v117, 0x42800000, v117
	v_mul_f32_e32 v118, 0x42800000, v118
	v_mul_f32_e32 v119, 0x42800000, v119
	v_mul_f32_e32 v120, 0x42800000, v120
	v_mul_f32_e32 v121, 0x42800000, v121
	v_mul_f32_e32 v122, 0x42800000, v122
	v_mul_f32_e32 v123, 0x42800000, v123
	v_mul_f32_e32 v124, 0x42800000, v124
	v_mul_f32_e32 v125, 0x42800000, v125
	v_mul_f32_e32 v126, 0x42800000, v126
	v_mul_f32_e32 v127, 0x42800000, v127
	v_med3_f32 v64, v64, s93, v224
	v_med3_f32 v65, v65, s93, v224
	v_med3_f32 v66, v66, s93, v224
	v_med3_f32 v67, v67, s93, v224
	v_med3_f32 v68, v68, s93, v224
	v_med3_f32 v69, v69, s93, v224
	v_med3_f32 v70, v70, s93, v224
	v_med3_f32 v71, v71, s93, v224
	v_med3_f32 v72, v72, s93, v224
	v_med3_f32 v73, v73, s93, v224
	v_med3_f32 v74, v74, s93, v224
	v_med3_f32 v75, v75, s93, v224
	v_med3_f32 v76, v76, s93, v224
	v_med3_f32 v77, v77, s93, v224
	v_med3_f32 v78, v78, s93, v224
	v_med3_f32 v79, v79, s93, v224
	v_med3_f32 v80, v80, s93, v224
	v_med3_f32 v81, v81, s93, v224
	v_med3_f32 v82, v82, s93, v224
	v_med3_f32 v83, v83, s93, v224
	v_med3_f32 v84, v84, s93, v224
	v_med3_f32 v85, v85, s93, v224
	v_med3_f32 v86, v86, s93, v224
	v_med3_f32 v87, v87, s93, v224
; __device__ __forceinline__ void cvt_finish(const CvtDesc& d, const float (&t)[64], LAS float* scr, int lane) {
;     LAS float* sw = scr + (lane >> 4) * 65 + 4 * (lane & 15);
; #pragma unroll
;     for (int i = 0; i < 16; ++i) { sw[(4 * i) * 65] = t[4 * i]; sw[(4 * i) * 65 + 1] = t[4 * i + 1]; sw[(4 * i) * 65 + 2] = t[4 * i + 2]; sw[(4 * i) * 65 + 3] = t[4 * i + 3]; }
;     LDS_WAIT();
;     const int c = lane & 7;
;     if (d.f8) {
; #pragma unroll
;         for (int j = 0; j < 8; ++j) { const int n = (lane >> 3) + 8 * j; const LAS float* s = scr + (8 * c) * 65 + n;
;             int a = __builtin_amdgcn_cvt_pk_fp8_f32(clamp8(s[0 * 65] * W8_SCALE), clamp8(s[1 * 65] * W8_SCALE), 0, false); a = __builtin_amdgcn_cvt_pk_fp8_f32(clamp8(s[2 * 65] * W8_SCALE), clamp8(s[3 * 65] * W8_SCALE), a, true);
;             int b = __builtin_amdgcn_cvt_pk_fp8_f32(clamp8(s[4 * 65] * W8_SCALE), clamp8(s[5 * 65] * W8_SCALE), 0, false); b = __builtin_amdgcn_cvt_pk_fp8_f32(clamp8(s[6 * 65] * W8_SCALE), clamp8(s[7 * 65] * W8_SCALE), b, true);
;             __builtin_nontemporal_store((u32x2){(unsigned)a, (unsigned)b}, (u32x2*)(d.dst + (size_t)n * d.dKB + 8 * c)); }
; __device__ __forceinline__ CvtDesc conv_expert_desc(const KA& a, unsigned char* ws, int q) {
;     const int l = q / Q_PER_L; int r = q - l * Q_PER_L;
;     unsigned char* wl = ws + WS_W + (size_t)l * W_LSTRIDE;
;     CvtDesc d; d.f8 = (MOE_FP8_LAST && (MOE_FP8_GU_ALL || l == NLAYER - 1)) ? 1 : 0;
;     if (MOE_FP8_LAST && MOE_FP8_DOWN_ALL && r >= 2 * Q_IG) d.f8 = 1;
;     const int eb = d.f8 ? 1 : 2;
;     if (r < 2 * Q_IG) { const int up = r >= Q_IG; if (up) r -= Q_IG; const int e = r >> 8, rr = r & 255, kb = rr >> 3, nb = rr & 7, n0 = nb * 64;
;         const float* src = e < 64 ? a.in(up ? 21 : 20) + ((size_t)l * 64 + e) * DM * FFE : a.in(up ? 24 : 23) + (size_t)l * DM * FFE;
;         d.src = src + (size_t)(kb * 64) * FFE + n0; d.N = FFE; d.dKB = DM * eb;
;         d.dst = wl + W_GU + ((size_t)e * 1024 * DM + (size_t)((n0 >> 7) * 256 + up * 128 + (n0 & 127)) * DM + kb * 64) * eb;
;     } else { r -= 2 * Q_IG; const int e = r >> 8, rr = r & 255, kb = rr >> 5, nb = rr & 31;
;         const float* src = e < 64 ? a.in(22) + ((size_t)l * 64 + e) * FFE * DM : a.in(25) + (size_t)l * FFE * DM;
;         d.src = src + (size_t)(kb * 64) * DM + nb * 64; d.N = DM; d.dKB = FFE * eb;
	v_med3_f32 v88, v88, s93, v224
	v_med3_f32 v89, v89, s93, v224
	v_med3_f32 v90, v90, s93, v224
	v_med3_f32 v91, v91, s93, v224
	v_med3_f32 v92, v92, s93, v224
	v_med3_f32 v93, v93, s93, v224
	v_med3_f32 v94, v94, s93, v224
	v_med3_f32 v95, v95, s93, v224
	v_med3_f32 v96, v96, s93, v224
	v_med3_f32 v97, v97, s93, v224
	v_med3_f32 v98, v98, s93, v224
	v_med3_f32 v99, v99, s93, v224
	v_med3_f32 v100, v100, s93, v224
	v_med3_f32 v101, v101, s93, v224
	v_med3_f32 v102, v102, s93, v224
	v_med3_f32 v103, v103, s93, v224
	v_med3_f32 v104, v104, s93, v224
	v_med3_f32 v105, v105, s93, v224
	v_med3_f32 v106, v106, s93, v224
	v_med3_f32 v107, v107, s93, v224
	v_med3_f32 v108, v108, s93, v224
	v_med3_f32 v109, v109, s93, v224
	v_med3_f32 v110, v110, s93, v224
	v_med3_f32 v111, v111, s93, v224
	v_med3_f32 v112, v112, s93, v224
	v_med3_f32 v113, v113, s93, v224
	v_med3_f32 v114, v114, s93, v224
	v_med3_f32 v115, v115, s93, v224
	v_med3_f32 v116, v116, s93, v224
	v_med3_f32 v117, v117, s93, v224
	v_med3_f32 v118, v118, s93, v224
	v_med3_f32 v119, v119, s93, v224
	v_med3_f32 v120, v120, s93, v224
	v_med3_f32 v121, v121, s93, v224
	v_med3_f32 v122, v122, s93, v224
	v_med3_f32 v123, v123, s93, v224
	v_med3_f32 v124, v124, s93, v224
	v_med3_f32 v125, v125, s93, v224
	v_med3_f32 v126, v126, s93, v224
	v_med3_f32 v127, v127, s93, v224
	v_cvt_pk_fp8_f32 v148, v64, v68
	v_cvt_pk_fp8_f32 v149, v80, v84
	v_cvt_pk_fp8_f32 v150, v96, v100
	v_cvt_pk_fp8_f32 v151, v112, v116
	v_cvt_pk_fp8_f32 v152, v65, v69
	v_cvt_pk_fp8_f32 v153, v81, v85
	v_cvt_pk_fp8_f32 v154, v97, v101
	v_cvt_pk_fp8_f32 v155, v113, v117
	v_cvt_pk_fp8_f32 v156, v66, v70
	v_cvt_pk_fp8_f32 v157, v82, v86
	v_cvt_pk_fp8_f32 v158, v98, v102
	v_cvt_pk_fp8_f32 v159, v114, v118
	v_cvt_pk_fp8_f32 v160, v67, v71
	v_cvt_pk_fp8_f32 v161, v83, v87
	v_cvt_pk_fp8_f32 v162, v99, v103
	v_cvt_pk_fp8_f32 v163, v115, v119
	v_cvt_pk_fp8_f32 v148, v72, v76 op_sel:[0,0,1]
	v_cvt_pk_fp8_f32 v149, v88, v92 op_sel:[0,0,1]
	v_cvt_pk_fp8_f32 v150, v104, v108 op_sel:[0,0,1]
	v_cvt_pk_fp8_f32 v151, v120, v124 op_sel:[0,0,1]
	v_cvt_pk_fp8_f32 v152, v73, v77 op_sel:[0,0,1]
	v_cvt_pk_fp8_f32 v153, v89, v93 op_sel:[0,0,1]
	v_cvt_pk_fp8_f32 v154, v105, v109 op_sel:[0,0,1]
	v_cvt_pk_fp8_f32 v155, v121, v125 op_sel:[0,0,1]
	v_cvt_pk_fp8_f32 v156, v74, v78 op_sel:[0,0,1]
	v_cvt_pk_fp8_f32 v157, v90, v94 op_sel:[0,0,1]
	v_cvt_pk_fp8_f32 v158, v106, v110 op_sel:[0,0,1]
	v_cvt_pk_fp8_f32 v159, v122, v126 op_sel:[0,0,1]
	v_cvt_pk_fp8_f32 v160, v75, v79 op_sel:[0,0,1]
	v_cvt_pk_fp8_f32 v161, v91, v95 op_sel:[0,0,1]
	v_cvt_pk_fp8_f32 v162, v107, v111 op_sel:[0,0,1]
	v_cvt_pk_fp8_f32 v163, v123, v127 op_sel:[0,0,1]
	s_movk_i32 s1, 0x200
	s_cmp_eq_u32 s18, 0
	s_cselect_b32 s0, 13, 11
	s_cselect_b32 s1, 0x800, s1
	v_lshlrev_b32_e32 v167, 4, v164
	v_lshl_add_u32 v167, v165, s0, v167
	global_store_dwordx4 v167, v[148:151], s[16:17] nt
	v_add_u32_e32 v167, s1, v167
	global_store_dwordx4 v167, v[152:155], s[16:17] nt
	v_add_u32_e32 v167, s1, v167
	global_store_dwordx4 v167, v[156:159], s[16:17] nt
	v_add_u32_e32 v167, s1, v167
	global_store_dwordx4 v167, v[160:163], s[16:17] nt
	s_nop 1
	s_add_u32 s20, s38, 24
	s_cmp_ge_u32 s20, 0xc300
	s_cselect_b32 s21, 1, 0
	s_cselect_b32 s0, 0xc300, 0
	s_sub_u32 s20, s20, s0
	s_cmp_ge_u32 s20, 0x8200
	s_cbranch_scc1 .Lcv_dn3
	s_cmp_ge_u32 s20, 0x4100
	s_cselect_b32 s22, 1, 0
	s_cselect_b32 s0, 0x4100, 0
	s_sub_u32 s20, s20, s0
	s_lshr_b32 s23, s20, 8
	s_lshl_b32 s31, s21, 6
	s_add_u32 s31, s31, s23
	s_cmp_eq_u32 s23, 64
	s_cselect_b32 s0, 3, 0
	s_cselect_b32 s31, s21, s31
	s_add_u32 s0, s0, s22
	s_lshl_b32 s0, s0, 1
	s_nop 0
	v_readlane_b32 s10, v147, s0
	s_or_b32 s0, s0, 1
	s_nop 0
	v_readlane_b32 s11, v147, s0
	s_lshr_b32 s33, s20, 3
	s_and_b32 s33, s33, 31
	s_and_b32 s34, s20, 7
	s_lshl_b32 s0, s33, 17
	s_lshl_b32 s1, s34, 8
	s_or_b32 s0, s0, s1
	s_lshl_b32 s1, s31, 22
	s_or_b32 s0, s0, s1
	s_lshr_b32 s1, s31, 10
	s_add_u32 s10, s10, s0
	s_addc_u32 s11, s11, s1
	s_lshr_b32 s0, s34, 1
	s_lshl_b32 s0, s0, 8
	s_lshl_b32 s1, s22, 7
	s_add_u32 s0, s0, s1
	s_and_b32 s1, s34, 1
	s_lshl_b32 s1, s1, 6
	s_add_u32 s0, s0, s1
	s_lshl_b32 s0, s0, 11
	s_lshl_b32 s1, s33, 6
	s_add_u32 s0, s0, s1
	s_lshl_b32 s1, s23, 21
	s_add_u32 s0, s0, s1
	s_add_u32 s0, s0, 0x2000000
	s_mul_i32 s1, s21, 0x1a800000
	s_add_u32 s0, s0, s1
	s_add_u32 s16, s28, s0
	s_addc_u32 s17, s29, 0
	s_mov_b32 s18, 0
	s_movk_i32 s15, 0x800
	s_mov_b32 s19, 15
	s_branch .Lcv_dd3

; #define LAS __attribute__((address_space(3)))
; __device__ __forceinline__ float clamp8(float x) { return __builtin_amdgcn_fmed3f(x, -448.f, 448.f); }
; #define LDS_WAIT() asm volatile("s_waitcnt lgkmcnt(0)" ::: "memory")
; __device__ __forceinline__ void cvt_load(const CvtDesc& d, float (&t)[64], int lane) {
;     const float* p = d.src + (size_t)(lane >> 4) * d.N + 4 * (lane & 15);
; #pragma unroll
;     for (int i = 0; i < 16; ++i) { const f32x4 v = __builtin_nontemporal_load((const f32x4*)(p + (size_t)(4 * i) * d.N));
;         t[4 * i] = v.x; t[4 * i + 1] = v.y; t[4 * i + 2] = v.z; t[4 * i + 3] = v.w; }
; }
; __device__ __forceinline__ void cvt_finish(const CvtDesc& d, const float (&t)[64], LAS float* scr, int lane) {
;     LAS float* sw = scr + (lane >> 4) * 65 + 4 * (lane & 15);
; #pragma unroll
;     for (int i = 0; i < 16; ++i) { sw[(4 * i) * 65] = t[4 * i]; sw[(4 * i) * 65 + 1] = t[4 * i + 1]; sw[(4 * i) * 65 + 2] = t[4 * i + 2]; sw[(4 * i) * 65 + 3] = t[4 * i + 3]; }
;     LDS_WAIT();
;     const int c = lane & 7;
;     if (d.f8) {
; #pragma unroll
;         for (int j = 0; j < 8; ++j) { const int n = (lane >> 3) + 8 * j; const LAS float* s = scr + (8 * c) * 65 + n;
;             int a = __builtin_amdgcn_cvt_pk_fp8_f32(clamp8(s[0 * 65] * W8_SCALE), clamp8(s[1 * 65] * W8_SCALE), 0, false); a = __builtin_amdgcn_cvt_pk_fp8_f32(clamp8(s[2 * 65] * W8_SCALE), clamp8(s[3 * 65] * W8_SCALE), a, true);
;             int b = __builtin_amdgcn_cvt_pk_fp8_f32(clamp8(s[4 * 65] * W8_SCALE), clamp8(s[5 * 65] * W8_SCALE), 0, false); b = __builtin_amdgcn_cvt_pk_fp8_f32(clamp8(s[6 * 65] * W8_SCALE), clamp8(s[7 * 65] * W8_SCALE), b, true);
.Lcv_dd3:
	v_lshlrev_b32_e32 v166, 4, v165
	v_lshl_add_u32 v166, v164, s19, v166
	global_load_dwordx4 v[64:67], v166, s[10:11] nt
	v_add_u32_e32 v166, s15, v166
	global_load_dwordx4 v[68:71], v166, s[10:11] nt
	v_add_u32_e32 v166, s15, v166
	global_load_dwordx4 v[72:75], v166, s[10:11] nt
	v_add_u32_e32 v166, s15, v166
	global_load_dwordx4 v[76:79], v166, s[10:11] nt
	v_add_u32_e32 v166, s15, v166
	global_load_dwordx4 v[80:83], v166, s[10:11] nt
	v_add_u32_e32 v166, s15, v166
	global_load_dwordx4 v[84:87], v166, s[10:11] nt
	v_add_u32_e32 v166, s15, v166
	global_load_dwordx4 v[88:91], v166, s[10:11] nt
	v_add_u32_e32 v166, s15, v166
	global_load_dwordx4 v[92:95], v166, s[10:11] nt
	v_add_u32_e32 v166, s15, v166
	global_load_dwordx4 v[96:99], v166, s[10:11] nt
	v_add_u32_e32 v166, s15, v166
	global_load_dwordx4 v[100:103], v166, s[10:11] nt
	v_add_u32_e32 v166, s15, v166
	global_load_dwordx4 v[104:107], v166, s[10:11] nt
	v_add_u32_e32 v166, s15, v166
	global_load_dwordx4 v[108:111], v166, s[10:11] nt
	v_add_u32_e32 v166, s15, v166
	global_load_dwordx4 v[112:115], v166, s[10:11] nt
	v_add_u32_e32 v166, s15, v166
	global_load_dwordx4 v[116:119], v166, s[10:11] nt
	v_add_u32_e32 v166, s15, v166
	global_load_dwordx4 v[120:123], v166, s[10:11] nt
	v_add_u32_e32 v166, s15, v166
	global_load_dwordx4 v[124:127], v166, s[10:11] nt
	s_waitcnt vmcnt(16)
	v_mul_f32_e32 v0, 0x42800000, v0
	v_mul_f32_e32 v1, 0x42800000, v1
	v_mul_f32_e32 v2, 0x42800000, v2
	v_mul_f32_e32 v3, 0x42800000, v3
	v_mul_f32_e32 v4, 0x42800000, v4
	v_mul_f32_e32 v5, 0x42800000, v5
	v_mul_f32_e32 v6, 0x42800000, v6
	v_mul_f32_e32 v7, 0x42800000, v7
	v_mul_f32_e32 v8, 0x42800000, v8
	v_mul_f32_e32 v9, 0x42800000, v9
	v_mul_f32_e32 v10, 0x42800000, v10
	v_mul_f32_e32 v11, 0x42800000, v11
	v_mul_f32_e32 v12, 0x42800000, v12
	v_mul_f32_e32 v13, 0x42800000, v13
	v_mul_f32_e32 v14, 0x42800000, v14
	v_mul_f32_e32 v15, 0x42800000, v15
	v_mul_f32_e32 v16, 0x42800000, v16
	v_mul_f32_e32 v17, 0x42800000, v17
	v_mul_f32_e32 v18, 0x42800000, v18
	v_mul_f32_e32 v19, 0x42800000, v19
	v_mul_f32_e32 v20, 0x42800000, v20
	v_mul_f32_e32 v21, 0x42800000, v21
	v_mul_f32_e32 v22, 0x42800000, v22
	v_mul_f32_e32 v23, 0x42800000, v23
	v_mul_f32_e32 v24, 0x42800000, v24
	v_mul_f32_e32 v25, 0x42800000, v25
	v_mul_f32_e32 v26, 0x42800000, v26
	v_mul_f32_e32 v27, 0x42800000, v27
	v_mul_f32_e32 v28, 0x42800000, v28
	v_mul_f32_e32 v29, 0x42800000, v29
	v_mul_f32_e32 v30, 0x42800000, v30
	v_mul_f32_e32 v31, 0x42800000, v31
	v_mul_f32_e32 v32, 0x42800000, v32
	v_mul_f32_e32 v33, 0x42800000, v33
	v_mul_f32_e32 v34, 0x42800000, v34
	v_mul_f32_e32 v35, 0x42800000, v35
	v_mul_f32_e32 v36, 0x42800000, v36
	v_mul_f32_e32 v37, 0x42800000, v37
	v_mul_f32_e32 v38, 0x42800000, v38
	v_mul_f32_e32 v39, 0x42800000, v39
	v_mul_f32_e32 v40, 0x42800000, v40
	v_mul_f32_e32 v41, 0x42800000, v41
	v_mul_f32_e32 v42, 0x42800000, v42
	v_mul_f32_e32 v43, 0x42800000, v43
	v_mul_f32_e32 v44, 0x42800000, v44
	v_mul_f32_e32 v45, 0x42800000, v45
	v_mul_f32_e32 v46, 0x42800000, v46
	v_mul_f32_e32 v47, 0x42800000, v47
	v_mul_f32_e32 v48, 0x42800000, v48
	v_mul_f32_e32 v49, 0x42800000, v49
	v_mul_f32_e32 v50, 0x42800000, v50
	v_mul_f32_e32 v51, 0x42800000, v51
	v_mul_f32_e32 v52, 0x42800000, v52
	v_mul_f32_e32 v53, 0x42800000, v53
	v_mul_f32_e32 v54, 0x42800000, v54
	v_mul_f32_e32 v55, 0x42800000, v55
	v_mul_f32_e32 v56, 0x42800000, v56
	v_mul_f32_e32 v57, 0x42800000, v57
	v_mul_f32_e32 v58, 0x42800000, v58
	v_mul_f32_e32 v59, 0x42800000, v59
	v_mul_f32_e32 v60, 0x42800000, v60
	v_mul_f32_e32 v61, 0x42800000, v61
	v_mul_f32_e32 v62, 0x42800000, v62
	v_mul_f32_e32 v63, 0x42800000, v63
	v_med3_f32 v0, v0, s93, v224
	v_med3_f32 v1, v1, s93, v224
	v_med3_f32 v2, v2, s93, v224
	v_med3_f32 v3, v3, s93, v224
	v_med3_f32 v4, v4, s93, v224
	v_med3_f32 v5, v5, s93, v224
	v_med3_f32 v6, v6, s93, v224
	v_med3_f32 v7, v7, s93, v224
	v_med3_f32 v8, v8, s93, v224
	v_med3_f32 v9, v9, s93, v224
	v_med3_f32 v10, v10, s93, v224
	v_med3_f32 v11, v11, s93, v224
	v_med3_f32 v12, v12, s93, v224
	v_med3_f32 v13, v13, s93, v224
	v_med3_f32 v14, v14, s93, v224
	v_med3_f32 v15, v15, s93, v224
	v_med3_f32 v16, v16, s93, v224
	v_med3_f32 v17, v17, s93, v224
	v_med3_f32 v18, v18, s93, v224
	v_med3_f32 v19, v19, s93, v224
	v_med3_f32 v20, v20, s93, v224
	v_med3_f32 v21, v21, s93, v224
	v_med3_f32 v22, v22, s93, v224
	v_med3_f32 v23, v23, s93, v224
	v_med3_f32 v24, v24, s93, v224
	v_med3_f32 v25, v25, s93, v224
	v_med3_f32 v26, v26, s93, v224
	v_med3_f32 v27, v27, s93, v224
	v_med3_f32 v28, v28, s93, v224
	v_med3_f32 v29, v29, s93, v224
	v_med3_f32 v30, v30, s93, v224
	v_med3_f32 v31, v31, s93, v224
	v_med3_f32 v32, v32, s93, v224
	v_med3_f32 v33, v33, s93, v224
	v_med3_f32 v34, v34, s93, v224
	v_med3_f32 v35, v35, s93, v224
	v_med3_f32 v36, v36, s93, v224
	v_med3_f32 v37, v37, s93, v224
	v_med3_f32 v38, v38, s93, v224
	v_med3_f32 v39, v39, s93, v224
	v_med3_f32 v40, v40, s93, v224
	v_med3_f32 v41, v41, s93, v224
	v_med3_f32 v42, v42, s93, v224
	v_med3_f32 v43, v43, s93, v224
	v_med3_f32 v44, v44, s93, v224
	v_med3_f32 v45, v45, s93, v224
	v_med3_f32 v46, v46, s93, v224
	v_med3_f32 v47, v47, s93, v224
	v_med3_f32 v48, v48, s93, v224
	v_med3_f32 v49, v49, s93, v224
	v_med3_f32 v50, v50, s93, v224
	v_med3_f32 v51, v51, s93, v224
	v_med3_f32 v52, v52, s93, v224
	v_med3_f32 v53, v53, s93, v224
	v_med3_f32 v54, v54, s93, v224
	v_med3_f32 v55, v55, s93, v224
	v_med3_f32 v56, v56, s93, v224
	v_med3_f32 v57, v57, s93, v224
	v_med3_f32 v58, v58, s93, v224
	v_med3_f32 v59, v59, s93, v224
	v_med3_f32 v60, v60, s93, v224
	v_med3_f32 v61, v61, s93, v224
	v_med3_f32 v62, v62, s93, v224
; #define LAS __attribute__((address_space(3)))
; __device__ __forceinline__ float clamp8(float x) { return __builtin_amdgcn_fmed3f(x, -448.f, 448.f); }
; #define LDS_WAIT() asm volatile("s_waitcnt lgkmcnt(0)" ::: "memory")
; __device__ __forceinline__ void cvt_finish(const CvtDesc& d, const float (&t)[64], LAS float* scr, int lane) {
;     LAS float* sw = scr + (lane >> 4) * 65 + 4 * (lane & 15);
; #pragma unroll
;     for (int i = 0; i < 16; ++i) { sw[(4 * i) * 65] = t[4 * i]; sw[(4 * i) * 65 + 1] = t[4 * i + 1]; sw[(4 * i) * 65 + 2] = t[4 * i + 2]; sw[(4 * i) * 65 + 3] = t[4 * i + 3]; }
;     LDS_WAIT();
;     const int c = lane & 7;
;     if (d.f8) {
; #pragma unroll
;         for (int j = 0; j < 8; ++j) { const int n = (lane >> 3) + 8 * j; const LAS float* s = scr + (8 * c) * 65 + n;
;             int a = __builtin_amdgcn_cvt_pk_fp8_f32(clamp8(s[0 * 65] * W8_SCALE), clamp8(s[1 * 65] * W8_SCALE), 0, false); a = __builtin_amdgcn_cvt_pk_fp8_f32(clamp8(s[2 * 65] * W8_SCALE), clamp8(s[3 * 65] * W8_SCALE), a, true);
;             int b = __builtin_amdgcn_cvt_pk_fp8_f32(clamp8(s[4 * 65] * W8_SCALE), clamp8(s[5 * 65] * W8_SCALE), 0, false); b = __builtin_amdgcn_cvt_pk_fp8_f32(clamp8(s[6 * 65] * W8_SCALE), clamp8(s[7 * 65] * W8_SCALE), b, true);
;             __builtin_nontemporal_store((u32x2){(unsigned)a, (unsigned)b}, (u32x2*)(d.dst + (size_t)n * d.dKB + 8 * c)); }
	v_med3_f32 v63, v63, s93, v224
	v_cvt_pk_fp8_f32 v148, v0, v4
	v_cvt_pk_fp8_f32 v149, v16, v20
	v_cvt_pk_fp8_f32 v150, v32, v36
	v_cvt_pk_fp8_f32 v151, v48, v52
	v_cvt_pk_fp8_f32 v152, v1, v5
	v_cvt_pk_fp8_f32 v153, v17, v21
	v_cvt_pk_fp8_f32 v154, v33, v37
	v_cvt_pk_fp8_f32 v155, v49, v53
	v_cvt_pk_fp8_f32 v156, v2, v6
	v_cvt_pk_fp8_f32 v157, v18, v22
	v_cvt_pk_fp8_f32 v158, v34, v38
	v_cvt_pk_fp8_f32 v159, v50, v54
	v_cvt_pk_fp8_f32 v160, v3, v7
	v_cvt_pk_fp8_f32 v161, v19, v23
	v_cvt_pk_fp8_f32 v162, v35, v39
	v_cvt_pk_fp8_f32 v163, v51, v55
	v_cvt_pk_fp8_f32 v148, v8, v12 op_sel:[0,0,1]
	v_cvt_pk_fp8_f32 v149, v24, v28 op_sel:[0,0,1]
	v_cvt_pk_fp8_f32 v150, v40, v44 op_sel:[0,0,1]
	v_cvt_pk_fp8_f32 v151, v56, v60 op_sel:[0,0,1]
	v_cvt_pk_fp8_f32 v152, v9, v13 op_sel:[0,0,1]
	v_cvt_pk_fp8_f32 v153, v25, v29 op_sel:[0,0,1]
	v_cvt_pk_fp8_f32 v154, v41, v45 op_sel:[0,0,1]
	v_cvt_pk_fp8_f32 v155, v57, v61 op_sel:[0,0,1]
	v_cvt_pk_fp8_f32 v156, v10, v14 op_sel:[0,0,1]
	v_cvt_pk_fp8_f32 v157, v26, v30 op_sel:[0,0,1]
	v_cvt_pk_fp8_f32 v158, v42, v46 op_sel:[0,0,1]
	v_cvt_pk_fp8_f32 v159, v58, v62 op_sel:[0,0,1]
	v_cvt_pk_fp8_f32 v160, v11, v15 op_sel:[0,0,1]
	v_cvt_pk_fp8_f32 v161, v27, v31 op_sel:[0,0,1]
	v_cvt_pk_fp8_f32 v162, v43, v47 op_sel:[0,0,1]
	v_cvt_pk_fp8_f32 v163, v59, v63 op_sel:[0,0,1]
	s_movk_i32 s1, 0x200
	s_cmp_eq_u32 s14, 0
	s_cselect_b32 s0, 13, 11
	s_cselect_b32 s1, 0x800, s1
	v_lshlrev_b32_e32 v167, 4, v164
	v_lshl_add_u32 v167, v165, s0, v167
	global_store_dwordx4 v167, v[148:151], s[12:13] nt
	v_add_u32_e32 v167, s1, v167
	global_store_dwordx4 v167, v[152:155], s[12:13] nt
	v_add_u32_e32 v167, s1, v167
	global_store_dwordx4 v167, v[156:159], s[12:13] nt
	v_add_u32_e32 v167, s1, v167
	global_store_dwordx4 v167, v[160:163], s[12:13] nt
	s_nop 1
	s_waitcnt vmcnt(0)
; #define LAS __attribute__((address_space(3)))
; __device__ __forceinline__ float clamp8(float x) { return __builtin_amdgcn_fmed3f(x, -448.f, 448.f); }
; #define LDS_WAIT() asm volatile("s_waitcnt lgkmcnt(0)" ::: "memory")
; __device__ __forceinline__ void cvt_finish(const CvtDesc& d, const float (&t)[64], LAS float* scr, int lane) {
;     LAS float* sw = scr + (lane >> 4) * 65 + 4 * (lane & 15);
; #pragma unroll
;     for (int i = 0; i < 16; ++i) { sw[(4 * i) * 65] = t[4 * i]; sw[(4 * i) * 65 + 1] = t[4 * i + 1]; sw[(4 * i) * 65 + 2] = t[4 * i + 2]; sw[(4 * i) * 65 + 3] = t[4 * i + 3]; }
;     LDS_WAIT();
;     const int c = lane & 7;
;     if (d.f8) {
; #pragma unroll
;         for (int j = 0; j < 8; ++j) { const int n = (lane >> 3) + 8 * j; const LAS float* s = scr + (8 * c) * 65 + n;
;             int a = __builtin_amdgcn_cvt_pk_fp8_f32(clamp8(s[0 * 65] * W8_SCALE), clamp8(s[1 * 65] * W8_SCALE), 0, false); a = __builtin_amdgcn_cvt_pk_fp8_f32(clamp8(s[2 * 65] * W8_SCALE), clamp8(s[3 * 65] * W8_SCALE), a, true);
;             int b = __builtin_amdgcn_cvt_pk_fp8_f32(clamp8(s[4 * 65] * W8_SCALE), clamp8(s[5 * 65] * W8_SCALE), 0, false); b = __builtin_amdgcn_cvt_pk_fp8_f32(clamp8(s[6 * 65] * W8_SCALE), clamp8(s[7 * 65] * W8_SCALE), b, true);
;             __builtin_nontemporal_store((u32x2){(unsigned)a, (unsigned)b}, (u32x2*)(d.dst + (size_t)n * d.dKB + 8 * c)); }
	v_mul_f32_e32 v64, 0x42800000, v64
	v_mul_f32_e32 v65, 0x42800000, v65
	v_mul_f32_e32 v66, 0x42800000, v66
	v_mul_f32_e32 v67, 0x42800000, v67
	v_mul_f32_e32 v68, 0x42800000, v68
	v_mul_f32_e32 v69, 0x42800000, v69
	v_mul_f32_e32 v70, 0x42800000, v70
	v_mul_f32_e32 v71, 0x42800000, v71
	v_mul_f32_e32 v72, 0x42800000, v72
	v_mul_f32_e32 v73, 0x42800000, v73
	v_mul_f32_e32 v74, 0x42800000, v74
	v_mul_f32_e32 v75, 0x42800000, v75
	v_mul_f32_e32 v76, 0x42800000, v76
	v_mul_f32_e32 v77, 0x42800000, v77
	v_mul_f32_e32 v78, 0x42800000, v78
	v_mul_f32_e32 v79, 0x42800000, v79
	v_mul_f32_e32 v80, 0x42800000, v80
	v_mul_f32_e32 v81, 0x42800000, v81
	v_mul_f32_e32 v82, 0x42800000, v82
	v_mul_f32_e32 v83, 0x42800000, v83
	v_mul_f32_e32 v84, 0x42800000, v84
	v_mul_f32_e32 v85, 0x42800000, v85
	v_mul_f32_e32 v86, 0x42800000, v86
	v_mul_f32_e32 v87, 0x42800000, v87
	v_mul_f32_e32 v88, 0x42800000, v88
	v_mul_f32_e32 v89, 0x42800000, v89
	v_mul_f32_e32 v90, 0x42800000, v90
	v_mul_f32_e32 v91, 0x42800000, v91
	v_mul_f32_e32 v92, 0x42800000, v92
	v_mul_f32_e32 v93, 0x42800000, v93
	v_mul_f32_e32 v94, 0x42800000, v94
	v_mul_f32_e32 v95, 0x42800000, v95
	v_mul_f32_e32 v96, 0x42800000, v96
	v_mul_f32_e32 v97, 0x42800000, v97
	v_mul_f32_e32 v98, 0x42800000, v98
	v_mul_f32_e32 v99, 0x42800000, v99
	v_mul_f32_e32 v100, 0x42800000, v100
	v_mul_f32_e32 v101, 0x42800000, v101
	v_mul_f32_e32 v102, 0x42800000, v102
	v_mul_f32_e32 v103, 0x42800000, v103
	v_mul_f32_e32 v104, 0x42800000, v104
	v_mul_f32_e32 v105, 0x42800000, v105
	v_mul_f32_e32 v106, 0x42800000, v106
	v_mul_f32_e32 v107, 0x42800000, v107
	v_mul_f32_e32 v108, 0x42800000, v108
	v_mul_f32_e32 v109, 0x42800000, v109
	v_mul_f32_e32 v110, 0x42800000, v110
	v_mul_f32_e32 v111, 0x42800000, v111
	v_mul_f32_e32 v112, 0x42800000, v112
	v_mul_f32_e32 v113, 0x42800000, v113
	v_mul_f32_e32 v114, 0x42800000, v114
	v_mul_f32_e32 v115, 0x42800000, v115
	v_mul_f32_e32 v116, 0x42800000, v116
	v_mul_f32_e32 v117, 0x42800000, v117
	v_mul_f32_e32 v118, 0x42800000, v118
	v_mul_f32_e32 v119, 0x42800000, v119
	v_mul_f32_e32 v120, 0x42800000, v120
	v_mul_f32_e32 v121, 0x42800000, v121
	v_mul_f32_e32 v122, 0x42800000, v122
	v_mul_f32_e32 v123, 0x42800000, v123
	v_mul_f32_e32 v124, 0x42800000, v124
	v_mul_f32_e32 v125, 0x42800000, v125
	v_mul_f32_e32 v126, 0x42800000, v126
	v_mul_f32_e32 v127, 0x42800000, v127
	v_med3_f32 v64, v64, s93, v224
	v_med3_f32 v65, v65, s93, v224
	v_med3_f32 v66, v66, s93, v224
	v_med3_f32 v67, v67, s93, v224
	v_med3_f32 v68, v68, s93, v224
	v_med3_f32 v69, v69, s93, v224
	v_med3_f32 v70, v70, s93, v224
	v_med3_f32 v71, v71, s93, v224
	v_med3_f32 v72, v72, s93, v224
	v_med3_f32 v73, v73, s93, v224
	v_med3_f32 v74, v74, s93, v224
	v_med3_f32 v75, v75, s93, v224
	v_med3_f32 v76, v76, s93, v224
	v_med3_f32 v77, v77, s93, v224
	v_med3_f32 v78, v78, s93, v224
	v_med3_f32 v79, v79, s93, v224
	v_med3_f32 v80, v80, s93, v224
	v_med3_f32 v81, v81, s93, v224
	v_med3_f32 v82, v82, s93, v224
	v_med3_f32 v83, v83, s93, v224
	v_med3_f32 v84, v84, s93, v224
	v_med3_f32 v85, v85, s93, v224
	v_med3_f32 v86, v86, s93, v224
	v_med3_f32 v87, v87, s93, v224
	v_med3_f32 v88, v88, s93, v224
	v_med3_f32 v89, v89, s93, v224
	v_med3_f32 v90, v90, s93, v224
	v_med3_f32 v91, v91, s93, v224
	v_med3_f32 v92, v92, s93, v224
	v_med3_f32 v93, v93, s93, v224
	v_med3_f32 v94, v94, s93, v224
	v_med3_f32 v95, v95, s93, v224
	v_med3_f32 v96, v96, s93, v224
	v_med3_f32 v97, v97, s93, v224
	v_med3_f32 v98, v98, s93, v224
	v_med3_f32 v99, v99, s93, v224
	v_med3_f32 v100, v100, s93, v224
	v_med3_f32 v101, v101, s93, v224
	v_med3_f32 v102, v102, s93, v224
	v_med3_f32 v103, v103, s93, v224
	v_med3_f32 v104, v104, s93, v224
	v_med3_f32 v105, v105, s93, v224
	v_med3_f32 v106, v106, s93, v224
	v_med3_f32 v107, v107, s93, v224
	v_med3_f32 v108, v108, s93, v224
	v_med3_f32 v109, v109, s93, v224
	v_med3_f32 v110, v110, s93, v224
	v_med3_f32 v111, v111, s93, v224
	v_med3_f32 v112, v112, s93, v224
	v_med3_f32 v113, v113, s93, v224
	v_med3_f32 v114, v114, s93, v224
	v_med3_f32 v115, v115, s93, v224
	v_med3_f32 v116, v116, s93, v224
	v_med3_f32 v117, v117, s93, v224
	v_med3_f32 v118, v118, s93, v224
	v_med3_f32 v119, v119, s93, v224
	v_med3_f32 v120, v120, s93, v224
	v_med3_f32 v121, v121, s93, v224
	v_med3_f32 v122, v122, s93, v224
	v_med3_f32 v123, v123, s93, v224
	v_med3_f32 v124, v124, s93, v224
	v_med3_f32 v125, v125, s93, v224
	v_med3_f32 v126, v126, s93, v224
	v_med3_f32 v127, v127, s93, v224
	v_cvt_pk_fp8_f32 v148, v64, v68
	v_cvt_pk_fp8_f32 v149, v80, v84
	v_cvt_pk_fp8_f32 v150, v96, v100
	v_cvt_pk_fp8_f32 v151, v112, v116
	v_cvt_pk_fp8_f32 v152, v65, v69
	v_cvt_pk_fp8_f32 v153, v81, v85
	v_cvt_pk_fp8_f32 v154, v97, v101
	v_cvt_pk_fp8_f32 v155, v113, v117
	v_cvt_pk_fp8_f32 v156, v66, v70
	v_cvt_pk_fp8_f32 v157, v82, v86
	v_cvt_pk_fp8_f32 v158, v98, v102
	v_cvt_pk_fp8_f32 v159, v114, v118
	v_cvt_pk_fp8_f32 v160, v67, v71
	v_cvt_pk_fp8_f32 v161, v83, v87
	v_cvt_pk_fp8_f32 v162, v99, v103
	v_cvt_pk_fp8_f32 v163, v115, v119
	v_cvt_pk_fp8_f32 v148, v72, v76 op_sel:[0,0,1]
	v_cvt_pk_fp8_f32 v149, v88, v92 op_sel:[0,0,1]
	v_cvt_pk_fp8_f32 v150, v104, v108 op_sel:[0,0,1]
	v_cvt_pk_fp8_f32 v151, v120, v124 op_sel:[0,0,1]
	v_cvt_pk_fp8_f32 v152, v73, v77 op_sel:[0,0,1]
	v_cvt_pk_fp8_f32 v153, v89, v93 op_sel:[0,0,1]
	v_cvt_pk_fp8_f32 v154, v105, v109 op_sel:[0,0,1]
	v_cvt_pk_fp8_f32 v155, v121, v125 op_sel:[0,0,1]
	v_cvt_pk_fp8_f32 v156, v74, v78 op_sel:[0,0,1]
	v_cvt_pk_fp8_f32 v157, v90, v94 op_sel:[0,0,1]
	v_cvt_pk_fp8_f32 v158, v106, v110 op_sel:[0,0,1]
	v_cvt_pk_fp8_f32 v159, v122, v126 op_sel:[0,0,1]
	v_cvt_pk_fp8_f32 v160, v75, v79 op_sel:[0,0,1]
	v_cvt_pk_fp8_f32 v161, v91, v95 op_sel:[0,0,1]
	v_cvt_pk_fp8_f32 v162, v107, v111 op_sel:[0,0,1]
	v_cvt_pk_fp8_f32 v163, v123, v127 op_sel:[0,0,1]
	s_movk_i32 s1, 0x200
	s_cmp_eq_u32 s18, 0
	s_cselect_b32 s0, 13, 11
	s_cselect_b32 s1, 0x800, s1
	v_lshlrev_b32_e32 v167, 4, v164
	v_lshl_add_u32 v167, v165, s0, v167
	global_store_dwordx4 v167, v[148:151], s[16:17] nt
	v_add_u32_e32 v167, s1, v167
	global_store_dwordx4 v167, v[152:155], s[16:17] nt
	v_add_u32_e32 v167, s1, v167
	global_store_dwordx4 v167, v[156:159], s[16:17] nt
	v_add_u32_e32 v167, s1, v167
	global_store_dwordx4 v167, v[160:163], s[16:17] nt
	s_nop 1
	s_branch .LBB0_779
